# v7 + GEMM phase prologue: second stage batch issued before the first counted wait (vmcnt 2 -> 8 after 14 loads)
# speedup vs baseline: 1.0043x; 1.0043x over previous
; #define PG8_STAGE(bufoff, gbase, voff) do { _Pragma("unroll") for (int _i = 0; _i < 2; ++_i) \
;         __builtin_amdgcn_global_load_lds((const unsigned*)((const char*)(gbase) + (voff)[_i]), (PG8_LAS unsigned*)(lds + (bufoff) + ldsw + _i * 8192), 16, 0, 0); } while (0)
; #define PG8_WAIT_V(n) asm volatile("s_waitcnt vmcnt(" #n ")" ::: "memory")
; #define PG8_BAR __builtin_amdgcn_s_barrier()
; template <class Epi, class Sched, bool ALIGN_EPI = false, bool SP2 = false, bool GATHER = false>
; __device__ __forceinline__ void gemm_phase(PG8_LAS unsigned char* lds, const Gemm g, const Sched& S, const Epi& E, int tid_in, const int* rowsrc = nullptr, PG8_LAS int* idx_lds = nullptr) {
;     ...
;     const char* cA = (const char*)g.A + (size_t)cur.pm * tstepA; const char* cB = (const char*)g.Bt + (size_t)cur.pn * tstep;
;     S.a_ready(cur);
;     if constexpr (SP2) {
;         PG8_STAGE(PG8_SB(0, 0), cB, voffB); PG8_STAGE(PG8_SB(0, 1), cB + hstep, voffB); PG8_STAGE(PG8_SA(0, 0), cA, PG8_OA(0)); PG8_STAGE(PG8_SA(0, 1), cA + hstepA, PG8_OA(1));
;         if (wr == 1) PG8_BAR;
;         PG8_WAIT_V(2); PG8_BAR;
;         PG8_STAGE(PG8_SB(1, 0), cB + kstep, voffB); PG8_STAGE(PG8_SA(1, 0), cA + kstep, PG8_OA(0)); PG8_STAGE(PG8_SB(1, 1), cB + hstep + kstep, voffB);
;         PG8_WAIT_V(6); PG8_BAR;
.LBB0_384:
	s_add_u32 s4, s4, 0xdc00000
	v_lshrrev_b32_e32 v18, 1, v16
	s_addc_u32 s5, s5, 0
	v_and_b32_e32 v18, 24, v18
	s_lshl_b32 s7, s7, 5
	v_and_b32_e32 v17, 15, v16
	v_lshlrev_b32_e32 v19, 1, v18
	v_lshlrev_b32_e32 v16, 2, v16
	s_and_b32 s12, s7, 0x60
	s_add_i32 m0, s29, 0x18000
	v_lshl_add_u64 v[8:9], v[8:9], 0, s[10:11]
	s_ashr_i32 s37, s2, 31
	v_lshl_or_b32 v148, s8, 6, v17
	v_lshl_or_b32 v17, v17, 6, v19
	s_lshl_b32 s8, s8, 13
	v_and_b32_e32 v16, 32, v16
	s_lshl_b32 s7, s12, 7
	global_load_lds_dwordx4 v[8:9], off
	v_lshl_add_u64 v[6:7], v[6:7], 0, s[10:11]
	s_add_i32 m0, s29, 0x1a000
	s_add_i32 s38, s29, 0x8000
	s_add_i32 s39, s29, 0xa000
	v_bitop3_b32 v19, v17, s8, v16 bitop3:0xde
	global_load_lds_dwordx4 v[6:7], off
	v_lshl_add_u64 v[2:3], v[2:3], 0, s[10:11]
	s_mov_b32 m0, s38
	s_add_u32 s8, s20, 0x40080
	global_load_lds_dwordx4 v[2:3], off
	v_lshl_add_u64 v[2:3], v[4:5], 0, s[10:11]
	s_mov_b32 m0, s39
	s_addc_u32 s9, s21, 0
	global_load_lds_dwordx4 v[2:3], off
	s_add_i32 m0, s29, 0x1c000
	v_lshl_add_u64 v[2:3], s[8:9], 0, v[0:1]
	global_load_lds_dwordx4 v[2:3], off
	v_lshl_add_u64 v[2:3], s[8:9], 0, v[130:131]
	s_add_i32 m0, s29, 0x1e000
	s_cmpk_lt_u32 s6, 0x100
	global_load_lds_dwordx4 v[2:3], off
	s_waitcnt vmcnt(8)
	s_barrier
	v_lshlrev_b32_e32 v2, 14, v14
	v_and_b32_e32 v2, 0xffff8000, v2
	v_lshl_add_u32 v2, v13, 11, v2
	v_and_b32_e32 v3, 1, v14
	v_lshl_or_b32 v2, v3, 6, v2
	v_lshl_add_u32 v136, v15, 1, v2
	v_lshlrev_b32_e32 v2, 14, v10
	v_and_b32_e32 v2, 0xffff8000, v2
	s_waitcnt vmcnt(6)
	v_lshl_add_u32 v2, v11, 11, v2
	v_and_b32_e32 v3, 1, v10
	v_lshl_or_b32 v2, v3, 6, v2
	v_readlane_b32 s8, v253, 11
	v_bitop3_b32 v149, v17, s7, v16 bitop3:0xde
	s_cselect_b64 s[6:7], -1, 0
	v_or_b32_e32 v150, s12, v18
	v_mov_b32_e32 v137, v1
	v_lshl_add_u32 v138, v12, 1, v2
	v_mov_b32_e32 v139, v1
	s_mov_b32 s41, 0
	v_add_u32_e32 v151, 0, v19
	v_readlane_b32 s43, v253, 10
	s_mov_b32 s45, s8
	s_barrier
	v_readlane_b32 s9, v253, 12
	s_branch .LBB0_387

; #define PG8_STAGE(bufoff, gbase, voff) do { _Pragma("unroll") for (int _i = 0; _i < 2; ++_i) \
;         __builtin_amdgcn_global_load_lds((const unsigned*)((const char*)(gbase) + (voff)[_i]), (PG8_LAS unsigned*)(lds + (bufoff) + ldsw + _i * 8192), 16, 0, 0); } while (0)
; #define PG8_WAIT_V(n) asm volatile("s_waitcnt vmcnt(" #n ")" ::: "memory")
; #define PG8_BAR __builtin_amdgcn_s_barrier()
; template <class Epi, class Sched, bool ALIGN_EPI = false, bool SP2 = false, bool GATHER = false>
; __device__ __forceinline__ void gemm_phase(PG8_LAS unsigned char* lds, const Gemm g, const Sched& S, const Epi& E, int tid_in, const int* rowsrc = nullptr, PG8_LAS int* idx_lds = nullptr) {
;     ...
;     const char* cA = (const char*)g.A + (size_t)cur.pm * tstepA; const char* cB = (const char*)g.Bt + (size_t)cur.pn * tstep;
;     S.a_ready(cur);
;     if constexpr (SP2) {
;         PG8_STAGE(PG8_SB(0, 0), cB, voffB); PG8_STAGE(PG8_SB(0, 1), cB + hstep, voffB); PG8_STAGE(PG8_SA(0, 0), cA, PG8_OA(0)); PG8_STAGE(PG8_SA(0, 1), cA + hstepA, PG8_OA(1));
;         if (wr == 1) PG8_BAR;
;         PG8_WAIT_V(2); PG8_BAR;
;         PG8_STAGE(PG8_SB(1, 0), cB + kstep, voffB); PG8_STAGE(PG8_SA(1, 0), cA + kstep, PG8_OA(0)); PG8_STAGE(PG8_SB(1, 1), cB + hstep + kstep, voffB);
;         PG8_WAIT_V(6); PG8_BAR;
.LBB0_609:
	v_readlane_b32 s12, v252, 32
	v_readlane_b32 s13, v252, 33
	s_add_u32 s47, s7, 0x35c00000
	s_mul_i32 s12, s12, 0xd800
	s_mov_b32 s13, s3
	s_addc_u32 s48, s8, 0
	s_lshl_b64 s[12:13], s[12:13], 2
	s_add_u32 s7, s7, s12
	s_addc_u32 s8, s8, s13
	s_add_u32 s49, s7, 0x102000
	v_lshrrev_b32_e32 v19, 1, v16
	s_addc_u32 s50, s8, 0
	v_and_b32_e32 v20, 24, v19
	s_lshl_b32 s5, s5, 5
	v_and_b32_e32 v17, 15, v16
	v_lshlrev_b32_e32 v19, 1, v20
	v_lshlrev_b32_e32 v16, 2, v16
	s_and_b32 s8, s5, 0x60
	s_add_i32 m0, s39, 0x18000
	v_lshl_add_u64 v[8:9], v[8:9], 0, s[10:11]
	s_ashr_i32 s51, s26, 31
	v_lshl_or_b32 v18, s6, 6, v17
	v_lshl_or_b32 v17, v17, 6, v19
	s_lshl_b32 s6, s6, 13
	v_and_b32_e32 v16, 32, v16
	s_lshl_b32 s5, s8, 7
	global_load_lds_dwordx4 v[8:9], off
	v_lshl_add_u64 v[6:7], v[6:7], 0, s[10:11]
	s_add_i32 m0, s39, 0x1a000
	s_add_i32 s52, s39, 0x8000
	s_add_i32 s53, s39, 0xa000
	v_bitop3_b32 v21, v17, s6, v16 bitop3:0xde
	global_load_lds_dwordx4 v[6:7], off
	v_lshl_add_u64 v[2:3], v[2:3], 0, s[10:11]
	s_mov_b32 m0, s52
	s_add_u32 s6, s22, 0x80080
	global_load_lds_dwordx4 v[2:3], off
	v_lshl_add_u64 v[2:3], v[4:5], 0, s[10:11]
	s_mov_b32 m0, s53
	s_addc_u32 s7, s23, 0
	global_load_lds_dwordx4 v[2:3], off
	s_add_i32 m0, s39, 0x1c000
	v_lshl_add_u64 v[2:3], s[6:7], 0, v[0:1]
	global_load_lds_dwordx4 v[2:3], off
	v_lshl_add_u64 v[2:3], s[6:7], 0, v[148:149]
	s_add_i32 m0, s39, 0x1e000
	v_ashrrev_i32_e32 v19, 31, v18
	global_load_lds_dwordx4 v[2:3], off
	s_waitcnt vmcnt(8)
	s_barrier
	v_or_b32_e32 v2, 16, v18
	v_ashrrev_i32_e32 v3, 31, v2
	v_lshlrev_b64 v[156:157], 11, v[2:3]
	v_or_b32_e32 v2, 32, v18
	v_ashrrev_i32_e32 v3, 31, v2
	v_lshlrev_b64 v[158:159], 11, v[2:3]
	v_or_b32_e32 v2, 48, v18
	v_ashrrev_i32_e32 v3, 31, v2
	v_lshlrev_b64 v[160:161], 11, v[2:3]
	v_lshlrev_b32_e32 v2, 15, v14
	v_and_b32_e32 v2, 0xffff0000, v2
	v_lshl_add_u32 v2, v13, 12, v2
	v_and_b32_e32 v3, 1, v14
	v_lshl_or_b32 v2, v3, 6, v2
	v_lshlrev_b64 v[154:155], 11, v[18:19]
	s_mov_b64 s[6:7], 0x40000
	v_lshl_add_u32 v170, v15, 1, v2
	v_lshlrev_b32_e32 v2, 15, v10
	v_lshl_add_u64 v[162:163], v[154:155], 0, s[6:7]
	s_mov_b64 s[6:7], 0x48000
	v_and_b32_e32 v2, 0xffff0000, v2
	s_waitcnt vmcnt(6)
	v_lshl_add_u64 v[164:165], v[154:155], 0, s[6:7]
	s_mov_b64 s[6:7], 0x50000
	v_lshl_add_u32 v2, v11, 12, v2
	v_and_b32_e32 v3, 1, v10
	s_cmpk_lt_u32 s4, 0x100
	v_lshl_add_u64 v[166:167], v[154:155], 0, s[6:7]
	s_mov_b64 s[6:7], 0x58000
	v_lshl_or_b32 v2, v3, 6, v2
	v_bitop3_b32 v184, v17, s5, v16 bitop3:0xde
	s_cselect_b64 s[4:5], -1, 0
	v_lshl_add_u64 v[168:169], v[154:155], 0, s[6:7]
	v_or_b32_e32 v185, s8, v20
	v_mov_b32_e32 v171, v1
	v_lshl_add_u32 v172, v12, 1, v2
	v_mov_b32_e32 v173, v1
	s_mov_b32 s54, 0
	v_add_u32_e32 v186, 0, v21
	s_barrier
	s_branch .LBB0_612

; #define PG8_STAGE(bufoff, gbase, voff) do { _Pragma("unroll") for (int _i = 0; _i < 2; ++_i) \
;         __builtin_amdgcn_global_load_lds((const unsigned*)((const char*)(gbase) + (voff)[_i]), (PG8_LAS unsigned*)(lds + (bufoff) + ldsw + _i * 8192), 16, 0, 0); } while (0)
; #define PG8_WAIT_V(n) asm volatile("s_waitcnt vmcnt(" #n ")" ::: "memory")
; #define PG8_BAR __builtin_amdgcn_s_barrier()
; template <class Epi, class Sched, bool ALIGN_EPI = false, bool SP2 = false, bool GATHER = false>
; __device__ __forceinline__ void gemm_phase(PG8_LAS unsigned char* lds, const Gemm g, const Sched& S, const Epi& E, int tid_in, const int* rowsrc = nullptr, PG8_LAS int* idx_lds = nullptr) {
;     ...
;     const char* cA = (const char*)g.A + (size_t)cur.pm * tstepA; const char* cB = (const char*)g.Bt + (size_t)cur.pn * tstep;
;     S.a_ready(cur);
;     if constexpr (SP2) {
;         PG8_STAGE(PG8_SB(0, 0), cB, voffB); PG8_STAGE(PG8_SB(0, 1), cB + hstep, voffB); PG8_STAGE(PG8_SA(0, 0), cA, PG8_OA(0)); PG8_STAGE(PG8_SA(0, 1), cA + hstepA, PG8_OA(1));
;         if (wr == 1) PG8_BAR;
;         PG8_WAIT_V(2); PG8_BAR;
;         PG8_STAGE(PG8_SB(1, 0), cB + kstep, voffB); PG8_STAGE(PG8_SA(1, 0), cA + kstep, PG8_OA(0)); PG8_STAGE(PG8_SB(1, 1), cB + hstep + kstep, voffB);
;         PG8_WAIT_V(6); PG8_BAR;
.LBB0_686:
	s_add_u32 s6, s6, 0xdc00000
	v_lshrrev_b32_e32 v18, 1, v16
	s_addc_u32 s7, s7, 0
	v_and_b32_e32 v18, 24, v18
	s_lshl_b32 s0, s0, 5
	v_and_b32_e32 v17, 15, v16
	v_lshlrev_b32_e32 v19, 1, v18
	v_lshlrev_b32_e32 v16, 2, v16
	s_and_b32 s12, s0, 0x60
	s_add_i32 m0, s31, 0x18000
	v_lshl_add_u64 v[8:9], v[8:9], 0, s[10:11]
	s_ashr_i32 s37, s2, 31
	v_lshl_or_b32 v144, s1, 6, v17
	v_lshl_or_b32 v17, v17, 6, v19
	s_lshl_b32 s1, s1, 13
	v_and_b32_e32 v16, 32, v16
	s_lshl_b32 s0, s12, 7
	global_load_lds_dwordx4 v[8:9], off
	v_lshl_add_u64 v[6:7], v[6:7], 0, s[10:11]
	s_add_i32 m0, s31, 0x1a000
	s_add_i32 s38, s31, 0x8000
	s_add_i32 s39, s31, 0xa000
	v_bitop3_b32 v145, v17, s0, v16 bitop3:0xde
	global_load_lds_dwordx4 v[6:7], off
	v_lshl_add_u64 v[2:3], v[2:3], 0, s[10:11]
	s_mov_b32 m0, s38
	s_add_u32 s0, s22, 0x40080
	v_bitop3_b32 v19, v17, s1, v16 bitop3:0xde
	global_load_lds_dwordx4 v[2:3], off
	v_lshl_add_u64 v[2:3], v[4:5], 0, s[10:11]
	s_mov_b32 m0, s39
	s_addc_u32 s1, s23, 0
	global_load_lds_dwordx4 v[2:3], off
	s_add_i32 m0, s31, 0x1c000
	v_lshl_add_u64 v[2:3], s[0:1], 0, v[0:1]
	global_load_lds_dwordx4 v[2:3], off
	v_lshl_add_u64 v[2:3], s[0:1], 0, v[130:131]
	s_add_i32 m0, s31, 0x1e000
	s_cmpk_lt_u32 s8, 0x100
	global_load_lds_dwordx4 v[2:3], off
	s_waitcnt vmcnt(8)
	s_barrier
	v_lshlrev_b32_e32 v2, 14, v14
	v_and_b32_e32 v2, 0xffff8000, v2
	v_lshl_add_u32 v2, v13, 11, v2
	v_and_b32_e32 v3, 1, v14
	v_lshl_or_b32 v2, v3, 6, v2
	v_lshl_add_u32 v136, v15, 1, v2
	v_lshlrev_b32_e32 v2, 14, v10
	v_and_b32_e32 v2, 0xffff8000, v2
	s_waitcnt vmcnt(6)
	v_lshl_add_u32 v2, v11, 11, v2
	v_and_b32_e32 v3, 1, v10
	v_lshl_or_b32 v2, v3, 6, v2
	v_readlane_b32 s0, v251, 59
	s_cselect_b64 s[8:9], -1, 0
	v_or_b32_e32 v148, s12, v18
	v_mov_b32_e32 v137, v1
	v_lshl_add_u32 v138, v12, 1, v2
	v_mov_b32_e32 v139, v1
	s_mov_b32 s41, 0
	v_add_u32_e32 v149, 0, v19
	v_readlane_b32 s43, v251, 58
	s_mov_b32 s45, s0
	s_barrier
	v_readlane_b32 s1, v251, 60
	s_branch .LBB0_689

; #define PG8_STAGE(bufoff, gbase, voff) do { _Pragma("unroll") for (int _i = 0; _i < 2; ++_i) \
;         __builtin_amdgcn_global_load_lds((const unsigned*)((const char*)(gbase) + (voff)[_i]), (PG8_LAS unsigned*)(lds + (bufoff) + ldsw + _i * 8192), 16, 0, 0); } while (0)
; #define PG8_WAIT_V(n) asm volatile("s_waitcnt vmcnt(" #n ")" ::: "memory")
; #define PG8_BAR __builtin_amdgcn_s_barrier()
; template <class Epi, class Sched, bool ALIGN_EPI = false, bool SP2 = false, bool GATHER = false>
; __device__ __forceinline__ void gemm_phase(PG8_LAS unsigned char* lds, const Gemm g, const Sched& S, const Epi& E, int tid_in, const int* rowsrc = nullptr, PG8_LAS int* idx_lds = nullptr) {
;     ...
;     const char* cA = (const char*)g.A + (size_t)cur.pm * tstepA; const char* cB = (const char*)g.Bt + (size_t)cur.pn * tstep;
;     S.a_ready(cur);
;     if constexpr (SP2) {
;         PG8_STAGE(PG8_SB(0, 0), cB, voffB); PG8_STAGE(PG8_SB(0, 1), cB + hstep, voffB); PG8_STAGE(PG8_SA(0, 0), cA, PG8_OA(0)); PG8_STAGE(PG8_SA(0, 1), cA + hstepA, PG8_OA(1));
;         if (wr == 1) PG8_BAR;
;         PG8_WAIT_V(2); PG8_BAR;
;         PG8_STAGE(PG8_SB(1, 0), cB + kstep, voffB); PG8_STAGE(PG8_SA(1, 0), cA + kstep, PG8_OA(0)); PG8_STAGE(PG8_SB(1, 1), cB + hstep + kstep, voffB);
;         PG8_WAIT_V(6); PG8_BAR;
.LBB0_1095:
	v_readlane_b32 s12, v252, 32
	v_readlane_b32 s13, v252, 33
	s_add_u32 s47, s7, 0x35c00000
	s_mul_i32 s12, s12, 0xd800
	s_mov_b32 s13, s3
	s_addc_u32 s48, s8, 0
	s_lshl_b64 s[12:13], s[12:13], 2
	s_add_u32 s7, s7, s12
	s_addc_u32 s8, s8, s13
	s_add_u32 s49, s7, 0x102000
	v_lshrrev_b32_e32 v19, 1, v16
	s_addc_u32 s50, s8, 0
	v_and_b32_e32 v20, 24, v19
	s_lshl_b32 s5, s5, 5
	v_and_b32_e32 v17, 15, v16
	v_lshlrev_b32_e32 v19, 1, v20
	v_lshlrev_b32_e32 v16, 2, v16
	s_and_b32 s8, s5, 0x60
	s_add_i32 m0, s39, 0x18000
	v_lshl_add_u64 v[8:9], v[8:9], 0, s[10:11]
	s_ashr_i32 s51, s26, 31
	v_lshl_or_b32 v18, s6, 6, v17
	v_lshl_or_b32 v17, v17, 6, v19
	s_lshl_b32 s6, s6, 13
	v_and_b32_e32 v16, 32, v16
	s_lshl_b32 s5, s8, 7
	global_load_lds_dwordx4 v[8:9], off
	v_lshl_add_u64 v[6:7], v[6:7], 0, s[10:11]
	s_add_i32 m0, s39, 0x1a000
	s_add_i32 s52, s39, 0x8000
	s_add_i32 s53, s39, 0xa000
	v_bitop3_b32 v21, v17, s6, v16 bitop3:0xde
	global_load_lds_dwordx4 v[6:7], off
	v_lshl_add_u64 v[2:3], v[2:3], 0, s[10:11]
	s_mov_b32 m0, s52
	s_add_u32 s6, s22, 0x40080
	global_load_lds_dwordx4 v[2:3], off
	v_lshl_add_u64 v[2:3], v[4:5], 0, s[10:11]
	s_mov_b32 m0, s53
	s_addc_u32 s7, s23, 0
	global_load_lds_dwordx4 v[2:3], off
	s_add_i32 m0, s39, 0x1c000
	v_lshl_add_u64 v[2:3], s[6:7], 0, v[0:1]
	global_load_lds_dwordx4 v[2:3], off
	v_lshl_add_u64 v[2:3], s[6:7], 0, v[148:149]
	s_add_i32 m0, s39, 0x1e000
	v_ashrrev_i32_e32 v19, 31, v18
	global_load_lds_dwordx4 v[2:3], off
	s_waitcnt vmcnt(8)
	s_barrier
	v_or_b32_e32 v2, 16, v18
	v_ashrrev_i32_e32 v3, 31, v2
	v_lshlrev_b64 v[156:157], 11, v[2:3]
	v_or_b32_e32 v2, 32, v18
	v_ashrrev_i32_e32 v3, 31, v2
	v_lshlrev_b64 v[158:159], 11, v[2:3]
	v_or_b32_e32 v2, 48, v18
	v_ashrrev_i32_e32 v3, 31, v2
	v_lshlrev_b64 v[160:161], 11, v[2:3]
	v_lshlrev_b32_e32 v2, 14, v14
	v_and_b32_e32 v2, 0xffff8000, v2
	v_lshl_add_u32 v2, v13, 11, v2
	v_and_b32_e32 v3, 1, v14
	v_lshl_or_b32 v2, v3, 6, v2
	v_lshlrev_b64 v[154:155], 11, v[18:19]
	s_mov_b64 s[6:7], 0x40000
	v_lshl_add_u32 v170, v15, 1, v2
	v_lshlrev_b32_e32 v2, 14, v10
	v_lshl_add_u64 v[162:163], v[154:155], 0, s[6:7]
	s_mov_b64 s[6:7], 0x48000
	v_and_b32_e32 v2, 0xffff8000, v2
	s_waitcnt vmcnt(6)
	v_lshl_add_u64 v[164:165], v[154:155], 0, s[6:7]
	s_mov_b64 s[6:7], 0x50000
	v_lshl_add_u32 v2, v11, 11, v2
	v_and_b32_e32 v3, 1, v10
	s_cmpk_lt_u32 s4, 0x100
	v_lshl_add_u64 v[166:167], v[154:155], 0, s[6:7]
	s_mov_b64 s[6:7], 0x58000
	v_lshl_or_b32 v2, v3, 6, v2
	v_bitop3_b32 v184, v17, s5, v16 bitop3:0xde
	s_cselect_b64 s[4:5], -1, 0
	v_lshl_add_u64 v[168:169], v[154:155], 0, s[6:7]
	v_or_b32_e32 v185, s8, v20
	v_mov_b32_e32 v171, v1
	v_lshl_add_u32 v172, v12, 1, v2
	v_mov_b32_e32 v173, v1
	s_mov_b32 s54, 0
	v_add_u32_e32 v186, 0, v21
	s_barrier
	s_branch .LBB0_1098

; #define PG8_STAGE(bufoff, gbase, voff) do { _Pragma("unroll") for (int _i = 0; _i < 2; ++_i) \
;         __builtin_amdgcn_global_load_lds((const unsigned*)((const char*)(gbase) + (voff)[_i]), (PG8_LAS unsigned*)(lds + (bufoff) + ldsw + _i * 8192), 16, 0, 0); } while (0)
; #define PG8_WAIT_V(n) asm volatile("s_waitcnt vmcnt(" #n ")" ::: "memory")
; #define PG8_BAR __builtin_amdgcn_s_barrier()
; template <class Epi, class Sched, bool ALIGN_EPI = false, bool SP2 = false, bool GATHER = false>
; __device__ __forceinline__ void gemm_phase(PG8_LAS unsigned char* lds, const Gemm g, const Sched& S, const Epi& E, int tid_in, const int* rowsrc = nullptr, PG8_LAS int* idx_lds = nullptr) {
;     ...
;     const char* cA = (const char*)g.A + (size_t)cur.pm * tstepA; const char* cB = (const char*)g.Bt + (size_t)cur.pn * tstep;
;     S.a_ready(cur);
;     if constexpr (SP2) {
;         PG8_STAGE(PG8_SB(0, 0), cB, voffB); PG8_STAGE(PG8_SB(0, 1), cB + hstep, voffB); PG8_STAGE(PG8_SA(0, 0), cA, PG8_OA(0)); PG8_STAGE(PG8_SA(0, 1), cA + hstepA, PG8_OA(1));
;         if (wr == 1) PG8_BAR;
;         PG8_WAIT_V(2); PG8_BAR;
;         PG8_STAGE(PG8_SB(1, 0), cB + kstep, voffB); PG8_STAGE(PG8_SA(1, 0), cA + kstep, PG8_OA(0)); PG8_STAGE(PG8_SB(1, 1), cB + hstep + kstep, voffB);
;         PG8_WAIT_V(6); PG8_BAR;
.LBB0_1121:
	s_add_u32 s6, s6, 0xdc00000
	v_lshrrev_b32_e32 v18, 1, v16
	s_addc_u32 s7, s7, 0
	v_and_b32_e32 v18, 24, v18
	s_lshl_b32 s0, s0, 5
	v_and_b32_e32 v17, 15, v16
	v_lshlrev_b32_e32 v19, 1, v18
	v_lshlrev_b32_e32 v16, 2, v16
	s_and_b32 s12, s0, 0x60
	s_add_i32 m0, s31, 0x18000
	v_lshl_add_u64 v[8:9], v[8:9], 0, s[10:11]
	s_ashr_i32 s37, s2, 31
	v_lshl_or_b32 v142, s1, 6, v17
	v_lshl_or_b32 v17, v17, 6, v19
	s_lshl_b32 s1, s1, 13
	v_and_b32_e32 v16, 32, v16
	s_lshl_b32 s0, s12, 7
	global_load_lds_dwordx4 v[8:9], off
	v_lshl_add_u64 v[6:7], v[6:7], 0, s[10:11]
	s_add_i32 m0, s31, 0x1a000
	s_add_i32 s38, s31, 0x8000
	s_add_i32 s39, s31, 0xa000
	v_bitop3_b32 v143, v17, s0, v16 bitop3:0xde
	global_load_lds_dwordx4 v[6:7], off
	v_lshl_add_u64 v[2:3], v[2:3], 0, s[10:11]
	s_mov_b32 m0, s38
	s_add_u32 s0, s22, 0x40080
	v_bitop3_b32 v19, v17, s1, v16 bitop3:0xde
	global_load_lds_dwordx4 v[2:3], off
	v_lshl_add_u64 v[2:3], v[4:5], 0, s[10:11]
	s_mov_b32 m0, s39
	s_addc_u32 s1, s23, 0
	global_load_lds_dwordx4 v[2:3], off
	s_add_i32 m0, s31, 0x1c000
	v_lshl_add_u64 v[2:3], s[0:1], 0, v[0:1]
	global_load_lds_dwordx4 v[2:3], off
	v_lshl_add_u64 v[2:3], s[0:1], 0, v[130:131]
	s_add_i32 m0, s31, 0x1e000
	s_cmpk_lt_u32 s8, 0x100
	global_load_lds_dwordx4 v[2:3], off
	s_waitcnt vmcnt(8)
	s_barrier
	v_lshlrev_b32_e32 v2, 14, v14
	v_and_b32_e32 v2, 0xffff8000, v2
	v_lshl_add_u32 v2, v13, 11, v2
	v_and_b32_e32 v3, 1, v14
	v_lshl_or_b32 v2, v3, 6, v2
	v_lshl_add_u32 v136, v15, 1, v2
	v_lshlrev_b32_e32 v2, 14, v10
	v_and_b32_e32 v2, 0xffff8000, v2
	s_waitcnt vmcnt(6)
	v_lshl_add_u32 v2, v11, 11, v2
	v_and_b32_e32 v3, 1, v10
	v_lshl_or_b32 v2, v3, 6, v2
	v_readlane_b32 s0, v253, 2
	s_cselect_b64 s[8:9], -1, 0
	v_or_b32_e32 v144, s12, v18
	v_mov_b32_e32 v137, v1
	v_lshl_add_u32 v138, v12, 1, v2
	v_mov_b32_e32 v139, v1
	s_mov_b32 s40, 0
	v_add_u32_e32 v145, 0, v19
	v_readlane_b32 s41, v253, 1
	s_mov_b32 s43, s0
	s_barrier
	v_readlane_b32 s1, v253, 3
	s_branch .LBB0_1124

; #define PG8_STAGE(bufoff, gbase, voff) do { _Pragma("unroll") for (int _i = 0; _i < 2; ++_i) \
;         __builtin_amdgcn_global_load_lds((const unsigned*)((const char*)(gbase) + (voff)[_i]), (PG8_LAS unsigned*)(lds + (bufoff) + ldsw + _i * 8192), 16, 0, 0); } while (0)
; #define PG8_WAIT_V(n) asm volatile("s_waitcnt vmcnt(" #n ")" ::: "memory")
; #define PG8_BAR __builtin_amdgcn_s_barrier()
; template <class Epi, class Sched, bool ALIGN_EPI = false, bool SP2 = false, bool GATHER = false>
; __device__ __forceinline__ void gemm_phase(PG8_LAS unsigned char* lds, const Gemm g, const Sched& S, const Epi& E, int tid_in, const int* rowsrc = nullptr, PG8_LAS int* idx_lds = nullptr) {
;     ...
;     const char* cA = (const char*)g.A + (size_t)cur.pm * tstepA; const char* cB = (const char*)g.Bt + (size_t)cur.pn * tstep;
;     S.a_ready(cur);
;     if constexpr (SP2) {
;         PG8_STAGE(PG8_SB(0, 0), cB, voffB); PG8_STAGE(PG8_SB(0, 1), cB + hstep, voffB); PG8_STAGE(PG8_SA(0, 0), cA, PG8_OA(0)); PG8_STAGE(PG8_SA(0, 1), cA + hstepA, PG8_OA(1));
;         if (wr == 1) PG8_BAR;
;         PG8_WAIT_V(2); PG8_BAR;
;         PG8_STAGE(PG8_SB(1, 0), cB + kstep, voffB); PG8_STAGE(PG8_SA(1, 0), cA + kstep, PG8_OA(0)); PG8_STAGE(PG8_SB(1, 1), cB + hstep + kstep, voffB);
;         PG8_WAIT_V(6); PG8_BAR;
.LBB0_1221:
	v_lshrrev_b32_e32 v18, 1, v16
	s_add_u32 s6, s30, 0x15400000
	v_and_b32_e32 v18, 24, v18
	s_addc_u32 s7, s31, 0
	v_and_b32_e32 v17, 15, v16
	v_lshlrev_b32_e32 v19, 1, v18
	v_lshlrev_b32_e32 v16, 2, v16
	s_lshl_b32 s1, s1, 5
	v_lshl_or_b32 v145, s8, 6, v17
	v_lshl_or_b32 v17, v17, 6, v19
	s_lshl_b32 s8, s8, 13
	v_and_b32_e32 v16, 32, v16
	s_and_b32 s1, s1, 0x60
	s_add_i32 m0, s17, 0x18000
	v_lshl_add_u64 v[8:9], v[8:9], 0, s[10:11]
	v_bitop3_b32 v19, v17, s8, v16 bitop3:0xde
	s_lshl_b32 s8, s1, 7
	global_load_lds_dwordx4 v[8:9], off
	v_lshl_add_u64 v[6:7], v[6:7], 0, s[10:11]
	s_add_i32 m0, s17, 0x1a000
	s_add_i32 s52, s17, 0x8000
	s_add_i32 s53, s17, 0xa000
	v_bitop3_b32 v148, v17, s8, v16 bitop3:0xde
	global_load_lds_dwordx4 v[6:7], off
	v_lshl_add_u64 v[2:3], v[2:3], 0, s[10:11]
	s_mov_b32 m0, s52
	s_add_u32 s8, s26, 0x20080
	global_load_lds_dwordx4 v[2:3], off
	v_lshl_add_u64 v[2:3], v[4:5], 0, s[10:11]
	s_mov_b32 m0, s53
	s_addc_u32 s9, s27, 0
	global_load_lds_dwordx4 v[2:3], off
	s_add_i32 m0, s17, 0x1c000
	v_lshl_add_u64 v[2:3], s[8:9], 0, v[0:1]
	global_load_lds_dwordx4 v[2:3], off
	v_lshl_add_u64 v[2:3], s[8:9], 0, v[130:131]
	s_add_i32 m0, s17, 0x1e000
	s_cmpk_lt_u32 s0, 0x100
	global_load_lds_dwordx4 v[2:3], off
	s_waitcnt vmcnt(8)
	s_barrier
	v_lshlrev_b32_e32 v2, 14, v14
	v_and_b32_e32 v2, 0xffff8000, v2
	v_lshl_add_u32 v2, v13, 11, v2
	v_and_b32_e32 v3, 1, v14
	v_lshl_or_b32 v2, v3, 6, v2
	v_lshl_add_u32 v136, v15, 1, v2
	v_lshlrev_b32_e32 v2, 14, v10
	v_and_b32_e32 v2, 0xffff8000, v2
	s_waitcnt vmcnt(6)
	v_lshl_add_u32 v2, v11, 11, v2
	v_and_b32_e32 v3, 1, v10
	v_lshl_or_b32 v2, v3, 6, v2
	s_cselect_b64 s[8:9], -1, 0
	v_or_b32_e32 v149, s1, v18
	v_mov_b32_e32 v137, v1
	v_lshl_add_u32 v138, v12, 1, v2
	v_mov_b32_e32 v139, v1
	s_mov_b32 s54, 0
	v_add_u32_e32 v150, 0, v19
	s_barrier
	s_branch .LBB0_1224

; #define PG8_STAGE(bufoff, gbase, voff) do { _Pragma("unroll") for (int _i = 0; _i < 2; ++_i) \
;         __builtin_amdgcn_global_load_lds((const unsigned*)((const char*)(gbase) + (voff)[_i]), (PG8_LAS unsigned*)(lds + (bufoff) + ldsw + _i * 8192), 16, 0, 0); } while (0)
; #define PG8_WAIT_V(n) asm volatile("s_waitcnt vmcnt(" #n ")" ::: "memory")
; #define PG8_BAR __builtin_amdgcn_s_barrier()
; template <class Epi, class Sched, bool ALIGN_EPI = false, bool SP2 = false, bool GATHER = false>
; __device__ __forceinline__ void gemm_phase(PG8_LAS unsigned char* lds, const Gemm g, const Sched& S, const Epi& E, int tid_in, const int* rowsrc = nullptr, PG8_LAS int* idx_lds = nullptr) {
;     ...
;     const char* cA = (const char*)g.A + (size_t)cur.pm * tstepA; const char* cB = (const char*)g.Bt + (size_t)cur.pn * tstep;
;     S.a_ready(cur);
;     if constexpr (SP2) {
;         PG8_STAGE(PG8_SB(0, 0), cB, voffB); PG8_STAGE(PG8_SB(0, 1), cB + hstep, voffB); PG8_STAGE(PG8_SA(0, 0), cA, PG8_OA(0)); PG8_STAGE(PG8_SA(0, 1), cA + hstepA, PG8_OA(1));
;         if (wr == 1) PG8_BAR;
;         PG8_WAIT_V(2); PG8_BAR;
;         PG8_STAGE(PG8_SB(1, 0), cB + kstep, voffB); PG8_STAGE(PG8_SA(1, 0), cA + kstep, PG8_OA(0)); PG8_STAGE(PG8_SB(1, 1), cB + hstep + kstep, voffB);
;         PG8_WAIT_V(6); PG8_BAR;
.LBB0_1239:
	v_lshrrev_b32_e32 v11, 1, v144
	v_and_b32_e32 v11, 24, v11
	v_and_b32_e32 v10, 15, v144
	v_lshlrev_b32_e32 v12, 1, v11
	v_lshl_or_b32 v138, s7, 6, v10
	v_lshl_or_b32 v10, v10, 6, v12
	v_lshlrev_b32_e32 v12, 2, v144
	s_sext_i32_i8 s60, s0
	s_lshl_b32 s0, s7, 13
	v_and_b32_e32 v12, 32, v12
	v_bitop3_b32 v13, v10, s0, v12 bitop3:0xde
	s_lshl_b32 s0, s6, 5
	s_and_b32 s0, s0, 0x60
	s_lshl_b32 s6, s0, 7
	v_bitop3_b32 v139, v10, s6, v12 bitop3:0xde
	s_add_u32 s6, s30, 0x1ba00000
	s_addc_u32 s7, s31, 0
	s_add_i32 m0, s21, 0x18000
	v_lshl_add_u64 v[8:9], v[8:9], 0, s[10:11]
	global_load_lds_dwordx4 v[8:9], off
	v_lshl_add_u64 v[6:7], v[6:7], 0, s[10:11]
	s_add_i32 m0, s21, 0x1a000
	s_add_i32 s57, s21, 0x8000
	s_add_i32 s58, s21, 0xa000
	global_load_lds_dwordx4 v[6:7], off
	v_lshl_add_u64 v[2:3], v[2:3], 0, s[10:11]
	s_mov_b32 m0, s57
	s_add_u32 s8, s22, 0x10080
	global_load_lds_dwordx4 v[2:3], off
	v_lshl_add_u64 v[2:3], v[4:5], 0, s[10:11]
	s_mov_b32 m0, s58
	s_addc_u32 s9, s23, 0
	global_load_lds_dwordx4 v[2:3], off
	s_add_i32 m0, s21, 0x1c000
	v_lshl_add_u64 v[2:3], s[8:9], 0, v[0:1]
	global_load_lds_dwordx4 v[2:3], off
	v_lshl_add_u64 v[2:3], s[8:9], 0, v[130:131]
	s_add_i32 m0, s21, 0x1e000
	s_cmpk_lt_u32 s1, 0x100
	global_load_lds_dwordx4 v[2:3], off
	s_waitcnt vmcnt(8)
	s_barrier
	s_waitcnt vmcnt(6)
	s_cselect_b64 s[8:9], -1, 0
	v_or_b32_e32 v140, s0, v11
	s_mov_b32 s59, 0
	v_add_u32_e32 v141, 0, v13
	s_barrier
	s_branch .LBB0_1242

; #define PG8_STAGE(bufoff, gbase, voff) do { _Pragma("unroll") for (int _i = 0; _i < 2; ++_i) \
;         __builtin_amdgcn_global_load_lds((const unsigned*)((const char*)(gbase) + (voff)[_i]), (PG8_LAS unsigned*)(lds + (bufoff) + ldsw + _i * 8192), 16, 0, 0); } while (0)
; #define PG8_WAIT_V(n) asm volatile("s_waitcnt vmcnt(" #n ")" ::: "memory")
; #define PG8_BAR __builtin_amdgcn_s_barrier()
; template <class Epi, class Sched, bool ALIGN_EPI = false, bool SP2 = false, bool GATHER = false>
; __device__ __forceinline__ void gemm_phase(PG8_LAS unsigned char* lds, const Gemm g, const Sched& S, const Epi& E, int tid_in, const int* rowsrc = nullptr, PG8_LAS int* idx_lds = nullptr) {
;     ...
;     const char* cA = (const char*)g.A + (size_t)cur.pm * tstepA; const char* cB = (const char*)g.Bt + (size_t)cur.pn * tstep;
;     S.a_ready(cur);
;     if constexpr (SP2) {
;         PG8_STAGE(PG8_SB(0, 0), cB, voffB); PG8_STAGE(PG8_SB(0, 1), cB + hstep, voffB); PG8_STAGE(PG8_SA(0, 0), cA, PG8_OA(0)); PG8_STAGE(PG8_SA(0, 1), cA + hstepA, PG8_OA(1));
;         if (wr == 1) PG8_BAR;
;         PG8_WAIT_V(2); PG8_BAR;
;         PG8_STAGE(PG8_SB(1, 0), cB + kstep, voffB); PG8_STAGE(PG8_SA(1, 0), cA + kstep, PG8_OA(0)); PG8_STAGE(PG8_SB(1, 1), cB + hstep + kstep, voffB);
;         PG8_WAIT_V(6); PG8_BAR;
.LBB0_1612:
	v_readlane_b32 s12, v252, 32
	v_readlane_b32 s13, v252, 33
	s_add_u32 s45, s7, 0x35c00000
	s_mul_i32 s12, s12, 0xd800
	s_mov_b32 s13, s3
	s_addc_u32 s47, s8, 0
	s_lshl_b64 s[12:13], s[12:13], 2
	s_add_u32 s7, s7, s12
	s_addc_u32 s8, s8, s13
	s_add_u32 s48, s7, 0x102000
	v_lshrrev_b32_e32 v19, 1, v16
	s_addc_u32 s49, s8, 0
	v_and_b32_e32 v20, 24, v19
	s_lshl_b32 s5, s5, 5
	v_and_b32_e32 v17, 15, v16
	v_lshlrev_b32_e32 v19, 1, v20
	v_lshlrev_b32_e32 v16, 2, v16
	s_and_b32 s8, s5, 0x60
	s_add_i32 m0, s39, 0x18000
	v_lshl_add_u64 v[8:9], v[8:9], 0, s[10:11]
	s_ashr_i32 s50, s26, 31
	v_lshl_or_b32 v18, s6, 6, v17
	v_lshl_or_b32 v17, v17, 6, v19
	s_lshl_b32 s6, s6, 13
	v_and_b32_e32 v16, 32, v16
	s_lshl_b32 s5, s8, 7
	global_load_lds_dwordx4 v[8:9], off
	v_lshl_add_u64 v[6:7], v[6:7], 0, s[10:11]
	s_add_i32 m0, s39, 0x1a000
	s_add_i32 s51, s39, 0x8000
	s_add_i32 s52, s39, 0xa000
	v_bitop3_b32 v21, v17, s6, v16 bitop3:0xde
	global_load_lds_dwordx4 v[6:7], off
	v_lshl_add_u64 v[2:3], v[2:3], 0, s[10:11]
	s_mov_b32 m0, s51
	s_add_u32 s6, s22, 0x40080
	global_load_lds_dwordx4 v[2:3], off
	v_lshl_add_u64 v[2:3], v[4:5], 0, s[10:11]
	s_mov_b32 m0, s52
	s_addc_u32 s7, s23, 0
	global_load_lds_dwordx4 v[2:3], off
	s_add_i32 m0, s39, 0x1c000
	v_lshl_add_u64 v[2:3], s[6:7], 0, v[0:1]
	global_load_lds_dwordx4 v[2:3], off
	v_lshl_add_u64 v[2:3], s[6:7], 0, v[148:149]
	s_add_i32 m0, s39, 0x1e000
	v_ashrrev_i32_e32 v19, 31, v18
	global_load_lds_dwordx4 v[2:3], off
	s_waitcnt vmcnt(8)
	s_barrier
	v_or_b32_e32 v2, 16, v18
	v_ashrrev_i32_e32 v3, 31, v2
	v_lshlrev_b64 v[156:157], 11, v[2:3]
	v_or_b32_e32 v2, 32, v18
	v_ashrrev_i32_e32 v3, 31, v2
	v_lshlrev_b64 v[158:159], 11, v[2:3]
	v_or_b32_e32 v2, 48, v18
	v_ashrrev_i32_e32 v3, 31, v2
	v_lshlrev_b64 v[160:161], 11, v[2:3]
	v_lshlrev_b32_e32 v2, 14, v14
	v_and_b32_e32 v2, 0xffff8000, v2
	v_lshl_add_u32 v2, v13, 11, v2
	v_and_b32_e32 v3, 1, v14
	v_lshl_or_b32 v2, v3, 6, v2
	v_lshlrev_b64 v[154:155], 11, v[18:19]
	s_mov_b64 s[6:7], 0x40000
	v_lshl_add_u32 v170, v15, 1, v2
	v_lshlrev_b32_e32 v2, 14, v10
	v_lshl_add_u64 v[162:163], v[154:155], 0, s[6:7]
	s_mov_b64 s[6:7], 0x48000
	v_and_b32_e32 v2, 0xffff8000, v2
	s_waitcnt vmcnt(6)
	v_lshl_add_u64 v[164:165], v[154:155], 0, s[6:7]
	s_mov_b64 s[6:7], 0x50000
	v_lshl_add_u32 v2, v11, 11, v2
	v_and_b32_e32 v3, 1, v10
	s_cmpk_lt_u32 s4, 0x100
	v_lshl_add_u64 v[166:167], v[154:155], 0, s[6:7]
	s_mov_b64 s[6:7], 0x58000
	v_lshl_or_b32 v2, v3, 6, v2
	v_bitop3_b32 v184, v17, s5, v16 bitop3:0xde
	s_cselect_b64 s[4:5], -1, 0
	v_lshl_add_u64 v[168:169], v[154:155], 0, s[6:7]
	v_or_b32_e32 v185, s8, v20
	v_mov_b32_e32 v171, v1
	v_lshl_add_u32 v172, v12, 1, v2
	v_mov_b32_e32 v173, v1
	s_mov_b32 s53, 0
	v_add_u32_e32 v186, 0, v21
	s_barrier
	s_branch .LBB0_1615

; #define PG8_STAGE(bufoff, gbase, voff) do { _Pragma("unroll") for (int _i = 0; _i < 2; ++_i) \
;         __builtin_amdgcn_global_load_lds((const unsigned*)((const char*)(gbase) + (voff)[_i]), (PG8_LAS unsigned*)(lds + (bufoff) + ldsw + _i * 8192), 16, 0, 0); } while (0)
; #define PG8_WAIT_V(n) asm volatile("s_waitcnt vmcnt(" #n ")" ::: "memory")
; #define PG8_BAR __builtin_amdgcn_s_barrier()
; template <class Epi, class Sched, bool ALIGN_EPI = false, bool SP2 = false, bool GATHER = false>
; __device__ __forceinline__ void gemm_phase(PG8_LAS unsigned char* lds, const Gemm g, const Sched& S, const Epi& E, int tid_in, const int* rowsrc = nullptr, PG8_LAS int* idx_lds = nullptr) {
;     ...
;     const char* cA = (const char*)g.A + (size_t)cur.pm * tstepA; const char* cB = (const char*)g.Bt + (size_t)cur.pn * tstep;
;     S.a_ready(cur);
;     if constexpr (SP2) {
;         PG8_STAGE(PG8_SB(0, 0), cB, voffB); PG8_STAGE(PG8_SB(0, 1), cB + hstep, voffB); PG8_STAGE(PG8_SA(0, 0), cA, PG8_OA(0)); PG8_STAGE(PG8_SA(0, 1), cA + hstepA, PG8_OA(1));
;         if (wr == 1) PG8_BAR;
;         PG8_WAIT_V(2); PG8_BAR;
;         PG8_STAGE(PG8_SB(1, 0), cB + kstep, voffB); PG8_STAGE(PG8_SA(1, 0), cA + kstep, PG8_OA(0)); PG8_STAGE(PG8_SB(1, 1), cB + hstep + kstep, voffB);
;         PG8_WAIT_V(6); PG8_BAR;
.LBB0_1922:
	v_lshrrev_b32_e32 v7, 1, v0
	s_mul_i32 s15, s15, s29
	v_and_b32_e32 v7, 24, v7
	s_lshl_b32 s6, s6, 5
	s_sub_i32 s14, s14, s15
	s_mul_i32 s9, s9, 17
	v_and_b32_e32 v6, 15, v0
	v_lshlrev_b32_e32 v8, 1, v7
	v_lshlrev_b32_e32 v0, 2, v0
	s_and_b32 s16, s6, 0x60
	s_add_i32 s19, s14, s9
	v_lshl_or_b32 v152, s7, 6, v6
	v_lshl_or_b32 v6, v6, 6, v8
	s_lshl_b32 s7, s7, 13
	v_and_b32_e32 v0, 32, v0
	s_lshl_b32 s6, s16, 7
	v_bitop3_b32 v153, v6, s6, v0 bitop3:0xde
	s_add_u32 s6, s27, 0x16400000
	v_bitop3_b32 v8, v6, s7, v0 bitop3:0xde
	s_addc_u32 s7, s28, 0
	s_add_u32 s14, s27, 0x9000080
	s_addc_u32 s15, s28, 0
	s_add_i32 m0, s45, 0x18000
	v_lshl_add_u64 v[4:5], v[4:5], 0, s[10:11]
	v_mov_b32_e32 v135, v1
	global_load_lds_dwordx4 v[4:5], off
	v_lshl_add_u64 v[2:3], v[2:3], 0, s[10:11]
	s_add_i32 m0, s45, 0x1a000
	s_add_i32 s49, s45, 0x8000
	v_mov_b32_e32 v137, v1
	global_load_lds_dwordx4 v[2:3], off
	v_lshl_add_u64 v[2:3], s[14:15], 0, v[134:135]
	s_mov_b32 m0, s49
	s_add_i32 s50, s45, 0xa000
	global_load_lds_dwordx4 v[2:3], off
	v_lshl_add_u64 v[2:3], s[14:15], 0, v[136:137]
	s_add_u32 s14, s20, 0x40080
	s_mov_b32 m0, s50
	s_addc_u32 s15, s21, 0
	global_load_lds_dwordx4 v[2:3], off
	s_add_i32 m0, s45, 0x1c000
	v_lshl_add_u64 v[2:3], s[14:15], 0, v[130:131]
	global_load_lds_dwordx4 v[2:3], off
	v_lshl_add_u64 v[2:3], s[14:15], 0, v[132:133]
	s_add_i32 m0, s45, 0x1e000
	s_cmpk_lt_u32 s8, 0x100
	global_load_lds_dwordx4 v[2:3], off
	s_waitcnt vmcnt(8)
	s_barrier
	s_waitcnt vmcnt(6)
	v_readlane_b32 s14, v253, 49
	s_cselect_b64 s[8:9], -1, 0
	s_add_u32 s12, s14, s12
	v_readlane_b32 s14, v253, 50
	v_or_b32_e32 v137, s16, v7
	s_addc_u32 s13, s14, s13
	s_mov_b32 s51, 0
	v_add_u32_e32 v154, 0, v8
	s_barrier
	s_branch .LBB0_1925

; #define PG8_STAGE(bufoff, gbase, voff) do { _Pragma("unroll") for (int _i = 0; _i < 2; ++_i) \
;         __builtin_amdgcn_global_load_lds((const unsigned*)((const char*)(gbase) + (voff)[_i]), (PG8_LAS unsigned*)(lds + (bufoff) + ldsw + _i * 8192), 16, 0, 0); } while (0)
; #define PG8_WAIT_V(n) asm volatile("s_waitcnt vmcnt(" #n ")" ::: "memory")
; #define PG8_BAR __builtin_amdgcn_s_barrier()
; template <class Epi, class Sched, bool ALIGN_EPI = false, bool SP2 = false, bool GATHER = false>
; __device__ __forceinline__ void gemm_phase(PG8_LAS unsigned char* lds, const Gemm g, const Sched& S, const Epi& E, int tid_in, const int* rowsrc = nullptr, PG8_LAS int* idx_lds = nullptr) {
;     ...
;     const char* cA = (const char*)g.A + (size_t)cur.pm * tstepA; const char* cB = (const char*)g.Bt + (size_t)cur.pn * tstep;
;     S.a_ready(cur);
;     if constexpr (SP2) {
;         PG8_STAGE(PG8_SB(0, 0), cB, voffB); PG8_STAGE(PG8_SB(0, 1), cB + hstep, voffB); PG8_STAGE(PG8_SA(0, 0), cA, PG8_OA(0)); PG8_STAGE(PG8_SA(0, 1), cA + hstepA, PG8_OA(1));
;         if (wr == 1) PG8_BAR;
;         PG8_WAIT_V(2); PG8_BAR;
;         PG8_STAGE(PG8_SB(1, 0), cB + kstep, voffB); PG8_STAGE(PG8_SA(1, 0), cA + kstep, PG8_OA(0)); PG8_STAGE(PG8_SB(1, 1), cB + hstep + kstep, voffB);
;         PG8_WAIT_V(6); PG8_BAR;
.LBB0_1999:
	s_add_u32 s4, s6, 0x1ec00000
	s_addc_u32 s5, s7, 0
	s_add_u32 s6, s6, 0xda00000
	v_lshrrev_b32_e32 v17, 1, v15
	s_addc_u32 s7, s7, 0
	v_and_b32_e32 v17, 24, v17
	s_lshl_b32 s9, s9, 5
	v_and_b32_e32 v16, 15, v15
	v_lshlrev_b32_e32 v18, 1, v17
	v_lshlrev_b32_e32 v15, 2, v15
	s_and_b32 s14, s9, 0x60
	s_add_i32 m0, s25, 0x18000
	v_lshl_add_u64 v[8:9], v[8:9], 0, s[10:11]
	v_lshl_or_b32 v150, s12, 6, v16
	v_lshl_or_b32 v16, v16, 6, v18
	s_lshl_b32 s12, s12, 13
	v_and_b32_e32 v15, 32, v15
	s_lshl_b32 s9, s14, 7
	global_load_lds_dwordx4 v[8:9], off
	v_lshl_add_u64 v[6:7], v[6:7], 0, s[10:11]
	s_add_i32 m0, s25, 0x1a000
	s_add_i32 s51, s25, 0x8000
	s_add_i32 s52, s25, 0xa000
	v_bitop3_b32 v18, v16, s12, v15 bitop3:0xde
	global_load_lds_dwordx4 v[6:7], off
	v_lshl_add_u64 v[2:3], v[2:3], 0, s[10:11]
	s_mov_b32 m0, s51
	s_add_u32 s12, s28, 0x40080
	global_load_lds_dwordx4 v[2:3], off
	v_lshl_add_u64 v[2:3], v[4:5], 0, s[10:11]
	s_mov_b32 m0, s52
	s_addc_u32 s13, s29, 0
	global_load_lds_dwordx4 v[2:3], off
	s_add_i32 m0, s25, 0x1c000
	v_lshl_add_u64 v[2:3], s[12:13], 0, v[134:135]
	global_load_lds_dwordx4 v[2:3], off
	v_lshl_add_u64 v[2:3], s[12:13], 0, v[130:131]
	s_add_i32 m0, s25, 0x1e000
	s_cmpk_lt_u32 s8, 0x100
	global_load_lds_dwordx4 v[2:3], off
	s_waitcnt vmcnt(8)
	s_barrier
	v_cvt_f32_u32_e32 v2, s35
	v_and_b32_e32 v3, 1, v13
	v_bitop3_b32 v151, v16, s9, v15 bitop3:0xde
	s_cselect_b64 s[8:9], -1, 0
	v_rcp_iflag_f32_e32 v2, v2
	s_sub_i32 s12, 0, s35
	s_waitcnt vmcnt(6)
	v_or_b32_e32 v152, s14, v17
	v_mul_f32_e32 v2, 0x4f7ffffe, v2
	v_cvt_u32_f32_e32 v2, v2
	s_mov_b32 s53, 0
	v_mov_b32_e32 v139, v1
	v_mov_b32_e32 v141, v1
	v_readfirstlane_b32 s13, v2
	v_lshlrev_b32_e32 v2, 14, v13
	v_and_b32_e32 v2, 0xffff8000, v2
	v_lshl_add_u32 v2, v12, 11, v2
	v_lshl_or_b32 v2, v3, 6, v2
	v_lshl_add_u32 v138, v14, 1, v2
	v_lshlrev_b32_e32 v2, 14, v0
	v_and_b32_e32 v2, 0xffff8000, v2
	s_mul_i32 s12, s12, s13
	v_lshl_add_u32 v2, v10, 11, v2
	v_and_b32_e32 v0, 1, v0
	s_mul_hi_u32 s12, s13, s12
	v_lshl_or_b32 v0, v0, 6, v2
	s_add_i32 s54, s13, s12
	v_lshl_add_u32 v140, v11, 1, v0
	v_add_u32_e32 v153, 0, v18
	s_barrier
	s_branch .LBB0_2002
